# speedup vs baseline: 1.0008x; 1.0004x over previous
.LBB13_6:
	s_or_b64 exec, exec, s[14:15]
	s_and_b32 s14, s3, 3
	v_lshl_or_b32 v80, s14, 14, v10
	s_waitcnt vmcnt(0)
	s_waitcnt lgkmcnt(0)
	s_barrier
	ds_read_b128 v[10:13], v80
	ds_read_b128 v[14:17], v80 offset:1024
	ds_read_b128 v[56:59], v80 offset:8192
	ds_read_b128 v[60:63], v80 offset:9216
	v_and_b32_e32 v98, 31, v0
	v_lshlrev_b32_e32 v82, 2, v98
	s_waitcnt lgkmcnt(2)
	v_mfma_f32_32x32x64_f8f6f4 v[16:31], v[10:17], v[2:9], 0
	ds_read_b128 v[64:67], v80 offset:2048
	ds_read_b128 v[68:71], v80 offset:3072
	ds_read_b128 v[72:75], v80 offset:10240
	ds_read_b128 v[76:79], v80 offset:11264
	s_lshr_b32 s16, s2, 3
	s_lshl_b32 s3, s21, 14
	s_and_b32 s16, s16, 0x1fffffe0
	s_add_i32 s3, s3, s16
	s_lshl_b32 s15, s14, 12
	s_add_i32 s3, s3, s19
	s_lshr_b32 s2, s2, 2
	v_lshrrev_b32_e32 v81, 5, v109
	s_and_b32 s2, s2, 32
	v_lshlrev_b32_e32 v111, 2, v81
	v_lshl_or_b32 v97, s14, 6, v111
	v_lshl_or_b32 v96, v81, 16, v82
	s_load_dwordx2 s[0:1], s[0:1], 0x70
	s_waitcnt lgkmcnt(0)
	v_mfma_f32_32x32x64_f8f6f4 v[0:15], v[56:63], v[2:9], 0
	ds_read_b128 v[88:91], v80 offset:4096
	ds_read_b128 v[92:95], v80 offset:5120
	ds_read_b128 v[114:117], v80 offset:12288
	ds_read_b128 v[118:121], v80 offset:13312
	ds_read_b128 v[100:103], v80 offset:6144
	ds_read_b128 v[104:107], v80 offset:7168
	ds_read_b128 v[56:59], v80 offset:14336
	ds_read_b128 v[60:63], v80 offset:15360
	s_waitcnt lgkmcnt(0)
	s_barrier
	global_load_dword v112, v82, s[8:9]
	global_load_dword v113, v82, s[10:11]
	s_add_i32 s8, s3, s15
	s_mov_b32 s9, 0
	s_lshl_b64 s[8:9], s[8:9], 6
	s_or_b32 s8, s8, s2
	s_lshl_b64 s[2:3], s[8:9], 2
	s_add_u32 s8, s12, s2
	v_lshlrev_b32_e32 v80, 2, v97
	s_addc_u32 s9, s13, s3
	s_lshl_b32 s10, s19, 2
	s_load_dword s4, s[4:5], s10 offset:0x0
	s_nop 0
	s_load_dword s5, s[6:7], s10 offset:0x0
	v_mfma_f32_32x32x64_f8f6f4 v[0:15], v[72:79], v[48:55], v[0:15]
	v_or_b32_e32 v99, 0x10800, v80
	v_or_b32_e32 v123, 0x11000, v80
	v_or_b32_e32 v124, 0x11800, v80
	v_or_b32_e32 v122, 0x10c00, v80
	v_or_b32_e32 v125, 0x11400, v80
	s_mul_i32 s6, s18, 0xa00
	v_mfma_f32_32x32x64_f8f6f4 v[16:31], v[64:71], v[48:55], v[16:31]
	v_or_b32_e32 v48, 0x10000, v80
	v_or_b32_e32 v49, 0x10400, v80
	ds_read_b128 v[52:55], v48
	ds_read_b128 v[84:87], v49
	v_mov_b32_e32 v48, v96
	ds_read_b128 v[64:67], v99
	ds_read_b128 v[68:71], v122
	ds_read_b128 v[72:75], v123
	ds_read_b128 v[76:79], v125
	ds_read_b128 v[80:83], v124
	global_load_dword v110, v48, s[8:9] nt
	v_add_u32_e32 v49, 0x4000, v48
	v_mfma_f32_32x32x64_f8f6f4 v[0:15], v[114:121], v[40:47], v[0:15]
	global_load_dword v120, v49, s[8:9] nt
	s_waitcnt lgkmcnt(0)
	v_mov_b32_e32 v114, s5
	v_mfma_f32_32x32x64_f8f6f4 v[16:31], v[88:95], v[40:47], v[16:31]
	v_add_u32_e32 v40, 0x8000, v48
	global_load_dword v121, v40, s[8:9] nt
	v_add_u32_e32 v40, 0xc000, v48
	global_load_dword v126, v40, s[8:9] nt
	v_mfma_f32_32x32x64_f8f6f4 v[16:31], v[100:107], v[32:39], v[16:31]
	v_fma_f32 v100, s4, v84, v114
	s_waitcnt vmcnt(4)
	v_fma_f32 v101, v112, v84, v113
	v_or_b32_e32 v84, 8, v97
	v_lshlrev_b32_e32 v102, 2, v84
	v_or_b32_e32 v40, 0x10000, v102
	v_or_b32_e32 v41, 0x10400, v102
	v_or_b32_e32 v104, 0x10800, v102
	v_or_b32_e32 v106, 0x11000, v102
	v_or_b32_e32 v108, 0x11800, v102
	ds_read_b128 v[92:95], v40
	ds_read_b128 v[88:91], v41
	v_or_b32_e32 v105, 0x10c00, v102
	ds_read_b128 v[40:43], v104
	ds_read_b128 v[44:47], v105
	v_mfma_f32_32x32x64_f8f6f4 v[0:15], v[56:63], v[32:39], v[0:15]
	v_mov_b32_e32 v56, v96
	v_or_b32_e32 v107, 0x11400, v102
	ds_read_b128 v[48:51], v106
	ds_read_b128 v[32:35], v107
	ds_read_b128 v[36:39], v108
	v_mul_f32_e32 v58, v100, v101
	v_add_u32_e32 v57, 0x20000, v56
	global_load_dword v57, v57, s[8:9] nt
	v_add_u32_e32 v59, 0x24000, v56
	global_load_dword v59, v59, s[8:9] nt
	v_add_u32_e32 v60, 0x28000, v56
	global_load_dword v60, v60, s[8:9] nt
	v_add_u32_e32 v56, 0x2c000, v56
	global_load_dword v56, v56, s[8:9] nt
	v_add_u32_e32 v100, 0x40000, v96
	global_load_dword v100, v100, s[8:9] nt
	v_add_u32_e32 v101, 0x44000, v96
	global_load_dword v101, v101, s[8:9] nt
	v_add_u32_e32 v102, 0x48000, v96
	global_load_dword v102, v102, s[8:9] nt
	v_add_u32_e32 v103, 0x4c000, v96
	global_load_dword v103, v103, s[8:9] nt
	v_mul_f32_e32 v58, 0xbfb8aa3b, v58
	v_exp_f32_e32 v58, v58
	v_fmamk_f32 v16, v16, 0x39800000, v52
	v_fma_f32 v52, v112, v85, v113
	v_fmamk_f32 v17, v17, 0x39800000, v53
	v_add_f32_e32 v58, 1.0, v58
	v_rcp_f32_e32 v58, v58
	v_fmac_f32_e32 v55, 0x39800000, v19
	s_waitcnt lgkmcnt(5)
	v_fma_f32 v19, v112, v89, v113
	v_fmac_f32_e32 v95, 0x39800000, v23
	s_waitcnt vmcnt(11)
	v_add_f32_e32 v16, v16, v110
	v_mul_f32_e32 v110, v16, v58
	v_fma_f32 v16, s4, v85, v114
	v_mul_f32_e32 v16, v16, v52
	v_mul_f32_e32 v16, 0xbfb8aa3b, v16
	v_exp_f32_e32 v16, v16
	v_fma_f32 v117, v72, v110, 0
	v_fma_f32 v118, v76, v110, 0
	s_waitcnt vmcnt(10)
	v_add_f32_e32 v17, v17, v120
	v_add_f32_e32 v16, 1.0, v16
	v_rcp_f32_e32 v16, v16
	v_fma_f32 v119, v80, v110, 0
	v_fma_f32 v115, v64, v110, 0
	v_fma_f32 v116, v68, v110, 0
	v_mul_f32_e32 v72, v17, v16
	v_fma_f32 v16, s4, v86, v114
	v_fma_f32 v17, v112, v86, v113
	v_mul_f32_e32 v16, v16, v17
	v_mul_f32_e32 v16, 0xbfb8aa3b, v16
	v_exp_f32_e32 v16, v16
	v_fmamk_f32 v17, v18, 0x39800000, v54
	v_fmac_f32_e32 v117, v73, v72
	v_fma_f32 v18, v112, v88, v113
	v_add_f32_e32 v16, 1.0, v16
	v_rcp_f32_e32 v16, v16
	s_waitcnt vmcnt(9)
	v_add_f32_e32 v17, v17, v121
	v_fmac_f32_e32 v118, v77, v72
	v_fmac_f32_e32 v119, v81, v72
	v_mul_f32_e32 v73, v17, v16
	v_fma_f32 v16, s4, v87, v114
	v_fma_f32 v17, v112, v87, v113
	v_mul_f32_e32 v16, v16, v17
	v_mul_f32_e32 v16, 0xbfb8aa3b, v16
	v_exp_f32_e32 v16, v16
	s_waitcnt vmcnt(8)
	v_add_f32_e32 v17, v55, v126
	v_fmac_f32_e32 v117, v74, v73
	v_or_b32_e32 v77, 16, v97
	v_add_f32_e32 v16, 1.0, v16
	v_rcp_f32_e32 v16, v16
	v_fmac_f32_e32 v115, v65, v72
	v_fmac_f32_e32 v116, v69, v72
	v_fmac_f32_e32 v119, v82, v73
	v_mul_f32_e32 v74, v17, v16
	v_fma_f32 v17, s4, v88, v114
	v_mul_f32_e32 v17, v17, v18
	v_mul_f32_e32 v17, 0xbfb8aa3b, v17
	v_fma_f32 v18, s4, v89, v114
	v_exp_f32_e32 v17, v17
	v_mul_f32_e32 v18, v18, v19
	v_mul_f32_e32 v18, 0xbfb8aa3b, v18
	v_exp_f32_e32 v18, v18
	v_add_f32_e32 v17, 1.0, v17
	v_rcp_f32_e32 v17, v17
	v_fmamk_f32 v16, v20, 0x39800000, v92
	v_add_f32_e32 v18, 1.0, v18
	v_rcp_f32_e32 v18, v18
	v_fmac_f32_e32 v117, v75, v74
	v_lshlrev_b32_e32 v52, 2, v77
	v_fmac_f32_e32 v115, v66, v73
	v_fmac_f32_e32 v116, v70, v73
	v_fmac_f32_e32 v118, v78, v73
	v_fmac_f32_e32 v119, v83, v74
	v_fma_f32 v85, s4, v90, v114
	s_waitcnt vmcnt(7)
	v_add_f32_e32 v16, v16, v57
	v_mul_f32_e32 v76, v16, v17
	v_fmamk_f32 v16, v21, 0x39800000, v93
	s_waitcnt vmcnt(6)
	v_add_f32_e32 v16, v16, v59
	v_mul_f32_e32 v75, v16, v18
	v_fmamk_f32 v16, v22, 0x39800000, v94
	s_waitcnt vmcnt(5)
	v_add_f32_e32 v83, v16, v60
	v_fma_f32 v86, v112, v90, v113
	v_or_b32_e32 v16, 0x10000, v52
	v_or_b32_e32 v17, 0x10400, v52
	v_or_b32_e32 v78, 0x10800, v52
	v_or_b32_e32 v80, 0x11000, v52
	v_or_b32_e32 v82, 0x11800, v52
	v_mov_b32_e32 v90, v96
	v_fmac_f32_e32 v115, v67, v74
	v_fmac_f32_e32 v116, v71, v74
	v_fmac_f32_e32 v118, v79, v74
	s_waitcnt vmcnt(4)
	v_add_f32_e32 v87, v95, v56
	v_fma_f32 v88, s4, v91, v114
	v_fma_f32 v89, v112, v91, v113
	ds_read_b128 v[56:59], v16
	ds_read_b128 v[68:71], v17
	v_or_b32_e32 v79, 0x10c00, v52
	ds_read_b128 v[64:67], v78
	ds_read_b128 v[60:63], v79
	v_or_b32_e32 v81, 0x11400, v52
	ds_read_b128 v[16:19], v80
	ds_read_b128 v[20:23], v81
	ds_read_b128 v[52:55], v82
	v_mul_f32_e32 v85, v85, v86
	v_mul_f32_e32 v88, v88, v89
	v_add_u32_e32 v120, 0x60000, v96
	global_load_dword v120, v120, s[8:9] nt
	v_add_u32_e32 v121, 0x64000, v96
	global_load_dword v121, v121, s[8:9] nt
	v_add_u32_e32 v126, 0x68000, v96
	global_load_dword v126, v126, s[8:9] nt
	v_add_u32_e32 v92, 0x6c000, v96
	global_load_dword v92, v92, s[8:9] nt
	s_waitcnt lgkmcnt(8)
	v_fmac_f32_e32 v118, v32, v76
	v_mul_f32_e32 v32, 0xbfb8aa3b, v85
	v_exp_f32_e32 v32, v32
	v_fmac_f32_e32 v118, v33, v75
	v_mul_f32_e32 v33, 0xbfb8aa3b, v88
	v_exp_f32_e32 v33, v33
	v_add_f32_e32 v32, 1.0, v32
	v_rcp_f32_e32 v32, v32
	s_waitcnt lgkmcnt(6)
	v_fmamk_f32 v24, v24, 0x39800000, v56
	v_fmac_f32_e32 v116, v44, v76
	v_fmac_f32_e32 v116, v45, v75
	v_mul_f32_e32 v85, v83, v32
	v_add_f32_e32 v32, 1.0, v33
	v_rcp_f32_e32 v32, v32
	s_waitcnt lgkmcnt(5)
	v_fma_f32 v33, v112, v68, v113
	v_fmac_f32_e32 v118, v34, v85
	v_fma_f32 v34, v112, v69, v113
	v_mul_f32_e32 v83, v87, v32
	v_fma_f32 v32, s4, v68, v114
	v_mul_f32_e32 v32, v32, v33
	v_mul_f32_e32 v32, 0xbfb8aa3b, v32
	v_exp_f32_e32 v32, v32
	v_fma_f32 v33, s4, v69, v114
	v_mul_f32_e32 v33, v33, v34
	v_mul_f32_e32 v33, 0xbfb8aa3b, v33
	v_add_f32_e32 v32, 1.0, v32
	v_rcp_f32_e32 v32, v32
	v_exp_f32_e32 v33, v33
	v_fmac_f32_e32 v116, v46, v85
	v_fmamk_f32 v25, v25, 0x39800000, v57
	v_fmac_f32_e32 v116, v47, v83
	v_fmac_f32_e32 v115, v40, v76
	v_fmac_f32_e32 v115, v41, v75
	v_fmac_f32_e32 v115, v42, v85
	v_fmac_f32_e32 v115, v43, v83
	v_fmac_f32_e32 v59, 0x39800000, v27
	v_fmac_f32_e32 v117, v48, v76
	v_fmac_f32_e32 v119, v36, v76
	v_fmac_f32_e32 v117, v49, v75
	v_fmac_f32_e32 v119, v37, v75
	v_fmac_f32_e32 v117, v50, v85
	v_fmac_f32_e32 v119, v38, v85
	v_fmac_f32_e32 v117, v51, v83
	v_fmac_f32_e32 v118, v35, v83
	v_fmac_f32_e32 v119, v39, v83
	v_mov_b32_e32 v94, v96
	s_waitcnt vmcnt(7)
	v_add_f32_e32 v24, v24, v100
	v_mul_f32_e32 v68, v24, v32
	v_add_f32_e32 v24, 1.0, v33
	v_rcp_f32_e32 v24, v24
	s_waitcnt vmcnt(6)
	v_add_f32_e32 v25, v25, v101
	s_waitcnt lgkmcnt(3)
	v_fmac_f32_e32 v116, v60, v68
	v_fma_f32 v32, v112, v71, v113
	v_mul_f32_e32 v60, v25, v24
	v_fma_f32 v24, s4, v70, v114
	v_fma_f32 v25, v112, v70, v113
	v_mul_f32_e32 v24, v24, v25
	v_mul_f32_e32 v24, 0xbfb8aa3b, v24
	v_exp_f32_e32 v24, v24
	v_fmamk_f32 v25, v26, 0x39800000, v58
	v_fma_f32 v26, s4, v71, v114
	v_mul_f32_e32 v26, v26, v32
	v_add_f32_e32 v24, 1.0, v24
	v_mul_f32_e32 v26, 0xbfb8aa3b, v26
	v_rcp_f32_e32 v24, v24
	v_exp_f32_e32 v26, v26
	s_waitcnt vmcnt(5)
	v_add_f32_e32 v25, v25, v102
	v_fmac_f32_e32 v115, v64, v68
	v_mul_f32_e32 v64, v25, v24
	v_add_f32_e32 v24, 1.0, v26
	v_rcp_f32_e32 v24, v24
	v_fmac_f32_e32 v116, v61, v60
	v_fmac_f32_e32 v116, v62, v64
	s_waitcnt vmcnt(4)
	v_add_f32_e32 v25, v59, v103
	v_or_b32_e32 v62, 24, v97
	v_fmac_f32_e32 v115, v65, v60
	v_mul_f32_e32 v61, v25, v24
	v_lshlrev_b32_e32 v24, 2, v62
	v_fmac_f32_e32 v115, v66, v64
	v_fmac_f32_e32 v116, v63, v61
	v_or_b32_e32 v25, 0x10000, v24
	v_or_b32_e32 v26, 0x10400, v24
	v_or_b32_e32 v63, 0x10800, v24
	v_or_b32_e32 v66, 0x11000, v24
	v_or_b32_e32 v69, 0x11800, v24
	v_mov_b32_e32 v70, v96
	v_fmac_f32_e32 v115, v67, v61
	ds_read_b128 v[48:51], v25
	ds_read_b128 v[56:59], v26
	v_or_b32_e32 v65, 0x10c00, v24
	ds_read_b128 v[44:47], v63
	ds_read_b128 v[32:35], v65
	v_or_b32_e32 v67, 0x11400, v24
	ds_read_b128 v[36:39], v66
	ds_read_b128 v[40:43], v67
	ds_read_b128 v[24:27], v69
	s_waitcnt lgkmcnt(9)
	v_fmac_f32_e32 v117, v16, v68
	v_add_u32_e32 v95, 0x80000, v96
	global_load_dword v95, v95, s[8:9] nt
	v_fmac_f32_e32 v117, v17, v60
	v_fmac_f32_e32 v117, v18, v64
	s_waitcnt lgkmcnt(5)
	v_fma_f32 v17, s4, v56, v114
	v_fma_f32 v18, v112, v56, v113
	v_mul_f32_e32 v17, v17, v18
	v_fmac_f32_e32 v117, v19, v61
	v_mul_f32_e32 v17, 0xbfb8aa3b, v17
	v_fma_f32 v18, s4, v57, v114
	v_fma_f32 v19, v112, v57, v113
	v_exp_f32_e32 v17, v17
	v_mul_f32_e32 v18, v18, v19
	v_mul_f32_e32 v18, 0xbfb8aa3b, v18
	v_exp_f32_e32 v18, v18
	v_add_f32_e32 v17, 1.0, v17
	v_rcp_f32_e32 v17, v17
	v_fmamk_f32 v16, v28, 0x39800000, v48
	v_add_f32_e32 v18, 1.0, v18
	v_rcp_f32_e32 v18, v18
	v_fma_f32 v19, v112, v59, v113
	v_fmac_f32_e32 v51, 0x39800000, v31
	v_fmac_f32_e32 v118, v20, v68
	v_fmac_f32_e32 v119, v52, v68
	v_fmac_f32_e32 v118, v21, v60
	v_fmac_f32_e32 v119, v53, v60
	v_fmac_f32_e32 v118, v22, v64
	v_fmac_f32_e32 v119, v54, v64
	v_fmac_f32_e32 v118, v23, v61
	v_fmac_f32_e32 v119, v55, v61
	s_waitcnt vmcnt(4)
	v_add_f32_e32 v16, v16, v120
	v_mul_f32_e32 v71, v16, v17
	v_fmamk_f32 v16, v29, 0x39800000, v49
	s_waitcnt vmcnt(3)
	v_add_f32_e32 v16, v16, v121
	v_mul_f32_e32 v70, v16, v18
	v_fma_f32 v17, s4, v58, v114
	v_fma_f32 v18, v112, v58, v113
	v_mul_f32_e32 v17, v17, v18
	v_fma_f32 v18, s4, v59, v114
	v_mul_f32_e32 v17, 0xbfb8aa3b, v17
	v_mul_f32_e32 v18, v18, v19
	v_exp_f32_e32 v17, v17
	v_mul_f32_e32 v18, 0xbfb8aa3b, v18
	v_exp_f32_e32 v18, v18
	v_fmamk_f32 v16, v30, 0x39800000, v50
	v_add_f32_e32 v17, 1.0, v17
	v_rcp_f32_e32 v17, v17
	v_add_f32_e32 v18, 1.0, v18
	v_rcp_f32_e32 v18, v18
	s_waitcnt vmcnt(2)
	v_add_f32_e32 v16, v16, v126
	v_mul_f32_e32 v88, v16, v17
	s_waitcnt vmcnt(1)
	v_add_f32_e32 v16, v51, v92
	v_or_b32_e32 v87, 32, v97
	v_mul_f32_e32 v86, v16, v18
	v_lshlrev_b32_e32 v16, 2, v87
	v_or_b32_e32 v17, 0x10000, v16
	v_or_b32_e32 v18, 0x10400, v16
	v_or_b32_e32 v89, 0x10800, v16
	v_or_b32_e32 v91, 0x11000, v16
	v_or_b32_e32 v93, 0x11800, v16
	ds_read_b128 v[28:31], v17
	ds_read_b128 v[100:103], v18
	v_or_b32_e32 v90, 0x10c00, v16
	ds_read_b128 v[52:55], v89
	ds_read_b128 v[48:51], v90
	v_or_b32_e32 v92, 0x11400, v16
	ds_read_b128 v[56:59], v91
	ds_read_b128 v[20:23], v92
	ds_read_b128 v[16:19], v93
	s_waitcnt lgkmcnt(11)
	v_fmac_f32_e32 v115, v44, v71
	v_add_u32_e32 v44, 0x84000, v94
	global_load_dword v44, v44, s[8:9] nt
	v_fmac_f32_e32 v115, v45, v70
	v_add_u32_e32 v45, 0x88000, v94
	global_load_dword v45, v45, s[8:9] nt
	v_fmac_f32_e32 v115, v46, v88
	v_add_u32_e32 v46, 0x8c000, v94
	global_load_dword v46, v46, s[8:9] nt
	v_add_u32_e32 v120, 0xa0000, v96
	global_load_dword v120, v120, s[8:9] nt
	v_add_u32_e32 v121, 0xa4000, v96
	global_load_dword v121, v121, s[8:9] nt
	v_add_u32_e32 v126, 0xa8000, v96
	global_load_dword v126, v126, s[8:9] nt
	s_waitcnt lgkmcnt(7)
	v_fmac_f32_e32 v119, v24, v71
	v_fmac_f32_e32 v119, v25, v70
	s_waitcnt lgkmcnt(5)
	v_fma_f32 v24, s4, v100, v114
	v_fma_f32 v25, v112, v100, v113
	v_mul_f32_e32 v24, v24, v25
	v_mul_f32_e32 v24, 0xbfb8aa3b, v24
	v_exp_f32_e32 v24, v24
	v_fmac_f32_e32 v119, v26, v88
	v_fma_f32 v25, s4, v101, v114
	v_fma_f32 v26, v112, v101, v113
	v_mul_f32_e32 v25, v25, v26
	v_add_f32_e32 v24, 1.0, v24
	v_mul_f32_e32 v25, 0xbfb8aa3b, v25
	v_rcp_f32_e32 v24, v24
	v_exp_f32_e32 v26, v25
	v_fmamk_f32 v0, v0, 0x39800000, v28
	v_fmamk_f32 v1, v1, 0x39800000, v29
	v_fmac_f32_e32 v116, v32, v71
	v_fmac_f32_e32 v117, v36, v71
	v_fmac_f32_e32 v116, v33, v70
	v_fmac_f32_e32 v117, v37, v70
	v_fmac_f32_e32 v116, v34, v88
	v_fmac_f32_e32 v117, v38, v88
	v_fmac_f32_e32 v115, v47, v86
	v_fmac_f32_e32 v116, v35, v86
	v_fmac_f32_e32 v117, v39, v86
	v_fmac_f32_e32 v119, v27, v86
	v_fmac_f32_e32 v31, 0x39800000, v3
	v_or_b32_e32 v27, 40, v97
	v_fmac_f32_e32 v118, v40, v71
	v_lshlrev_b32_e32 v33, 2, v27
	v_fmac_f32_e32 v118, v41, v70
	v_or_b32_e32 v29, 0x10400, v33
	v_fmac_f32_e32 v118, v42, v88
	v_or_b32_e32 v32, 0x11400, v33
	v_fmac_f32_e32 v118, v43, v86
	s_waitcnt vmcnt(6)
	v_add_f32_e32 v0, v0, v95
	v_mul_f32_e32 v25, v0, v24
	v_add_f32_e32 v0, 1.0, v26
	v_rcp_f32_e32 v0, v0
	s_waitcnt vmcnt(5)
	v_add_f32_e32 v1, v1, v44
	v_fma_f32 v26, v112, v103, v113
	s_waitcnt lgkmcnt(4)
	v_fmac_f32_e32 v115, v52, v25
	v_mul_f32_e32 v24, v1, v0
	v_fma_f32 v0, s4, v102, v114
	v_fma_f32 v1, v112, v102, v113
	v_mul_f32_e32 v0, v0, v1
	v_mul_f32_e32 v0, 0xbfb8aa3b, v0
	v_exp_f32_e32 v0, v0
	v_fmamk_f32 v1, v2, 0x39800000, v30
	v_fma_f32 v2, s4, v103, v114
	v_mul_f32_e32 v2, v2, v26
	v_add_u32_e32 v103, 0xac000, v96
	global_load_dword v103, v103, s[8:9] nt
	v_add_f32_e32 v0, 1.0, v0
	v_mul_f32_e32 v2, 0xbfb8aa3b, v2
	v_rcp_f32_e32 v0, v0
	v_exp_f32_e32 v2, v2
	s_waitcnt vmcnt(5)
	v_add_f32_e32 v1, v1, v45
	s_waitcnt lgkmcnt(3)
	v_fmac_f32_e32 v116, v48, v25
	v_mul_f32_e32 v28, v1, v0
	v_add_f32_e32 v0, 1.0, v2
	v_rcp_f32_e32 v0, v0
	s_waitcnt lgkmcnt(2)
	v_fmac_f32_e32 v117, v56, v25
	s_waitcnt vmcnt(4)
	v_add_f32_e32 v1, v31, v46
	v_fmac_f32_e32 v115, v53, v24
	v_fmac_f32_e32 v116, v49, v24
	v_fmac_f32_e32 v117, v57, v24
	v_mul_f32_e32 v26, v1, v0
	v_or_b32_e32 v0, 0x10000, v33
	v_fmac_f32_e32 v115, v54, v28
	v_fmac_f32_e32 v116, v50, v28
	v_fmac_f32_e32 v117, v58, v28
	ds_read_b128 v[0:3], v0
	ds_read_b128 v[34:37], v29
	v_or_b32_e32 v29, 0x10800, v33
	v_or_b32_e32 v30, 0x10c00, v33
	v_or_b32_e32 v31, 0x11000, v33
	v_or_b32_e32 v33, 0x11800, v33
	v_mov_b32_e32 v58, v96
	v_fmac_f32_e32 v115, v55, v26
	v_fmac_f32_e32 v116, v51, v26
	v_fmac_f32_e32 v117, v59, v26
	ds_read_b128 v[38:41], v29
	ds_read_b128 v[42:45], v30
	ds_read_b128 v[46:49], v31
	ds_read_b128 v[50:53], v32
	ds_read_b128 v[54:57], v33
	s_waitcnt lgkmcnt(8)
	v_fmac_f32_e32 v118, v20, v25
	v_add_u32_e32 v100, 0xc4000, v96
	global_load_dword v100, v100, s[8:9] nt
	v_add_u32_e32 v101, 0xc8000, v96
	global_load_dword v101, v101, s[8:9] nt
	v_add_u32_e32 v102, 0xcc000, v96
	global_load_dword v102, v102, s[8:9] nt
	v_fmac_f32_e32 v118, v21, v24
	s_waitcnt lgkmcnt(5)
	v_fma_f32 v20, s4, v34, v114
	v_fma_f32 v21, v112, v34, v113
	v_mul_f32_e32 v20, v20, v21
	v_mul_f32_e32 v20, 0xbfb8aa3b, v20
	v_exp_f32_e32 v20, v20
	v_fmac_f32_e32 v119, v16, v25
	v_fmamk_f32 v0, v4, 0x39800000, v0
	v_fma_f32 v4, v112, v35, v113
	v_add_f32_e32 v16, 1.0, v20
	v_rcp_f32_e32 v16, v16
	v_fmamk_f32 v1, v5, 0x39800000, v1
	v_fmac_f32_e32 v118, v22, v28
	v_fmac_f32_e32 v3, 0x39800000, v7
	v_or_b32_e32 v34, 48, v97
	v_fmac_f32_e32 v118, v23, v26
	v_fmac_f32_e32 v119, v17, v24
	v_fmac_f32_e32 v119, v18, v28
	v_fmac_f32_e32 v119, v19, v26
	s_waitcnt vmcnt(6)
	v_add_f32_e32 v0, v0, v120
	v_mul_f32_e32 v20, v0, v16
	v_fma_f32 v0, s4, v35, v114
	v_mul_f32_e32 v0, v0, v4
	v_mul_f32_e32 v0, 0xbfb8aa3b, v0
	v_exp_f32_e32 v0, v0
	s_waitcnt vmcnt(5)
	v_add_f32_e32 v1, v1, v121
	s_waitcnt lgkmcnt(4)
	v_fmac_f32_e32 v115, v38, v20
	s_waitcnt lgkmcnt(3)
	v_fmac_f32_e32 v116, v42, v20
	v_add_f32_e32 v0, 1.0, v0
	v_rcp_f32_e32 v0, v0
	s_waitcnt lgkmcnt(0)
	v_fmac_f32_e32 v119, v54, v20
	v_fmac_f32_e32 v117, v46, v20
	v_fmac_f32_e32 v118, v50, v20
	v_mul_f32_e32 v21, v1, v0
	v_fma_f32 v0, s4, v36, v114
	v_fma_f32 v1, v112, v36, v113
	v_mul_f32_e32 v0, v0, v1
	v_mul_f32_e32 v0, 0xbfb8aa3b, v0
	v_exp_f32_e32 v0, v0
	v_fmamk_f32 v1, v6, 0x39800000, v2
	s_waitcnt vmcnt(4)
	v_add_f32_e32 v1, v1, v126
	v_fmac_f32_e32 v115, v39, v21
	v_add_f32_e32 v0, 1.0, v0
	v_rcp_f32_e32 v0, v0
	v_lshlrev_b32_e32 v39, 2, v34
	v_fmac_f32_e32 v116, v43, v21
	v_or_b32_e32 v4, 0x10400, v39
	v_mul_f32_e32 v22, v1, v0
	v_fma_f32 v0, s4, v37, v114
	v_fma_f32 v1, v112, v37, v113
	v_mul_f32_e32 v0, v0, v1
	v_mul_f32_e32 v0, 0xbfb8aa3b, v0
	v_exp_f32_e32 v0, v0
	s_waitcnt vmcnt(3)
	v_add_f32_e32 v1, v3, v103
	v_add_u32_e32 v103, 0xc0000, v96
	global_load_dword v103, v103, s[8:9] nt
	v_fmac_f32_e32 v115, v40, v22
	v_fmac_f32_e32 v119, v55, v21
	v_add_f32_e32 v0, 1.0, v0
	v_rcp_f32_e32 v0, v0
	v_fmac_f32_e32 v117, v47, v21
	v_fmac_f32_e32 v118, v51, v21
	v_fmac_f32_e32 v119, v56, v22
	v_mul_f32_e32 v23, v1, v0
	v_or_b32_e32 v0, 0x10000, v39
	v_fmac_f32_e32 v115, v41, v23
	ds_read_b128 v[0:3], v0
	ds_read_b128 v[40:43], v4
	v_fmac_f32_e32 v116, v44, v22
	v_fmac_f32_e32 v117, v48, v22
	v_fmac_f32_e32 v118, v52, v22
	v_fmac_f32_e32 v119, v57, v23
	v_or_b32_e32 v35, 0x10800, v39
	v_or_b32_e32 v36, 0x10c00, v39
	v_or_b32_e32 v37, 0x11000, v39
	v_or_b32_e32 v38, 0x11400, v39
	s_waitcnt lgkmcnt(0)
	v_fma_f32 v57, s4, v41, v114
	v_fma_f32 v58, v112, v41, v113
	v_or_b32_e32 v41, 0x11800, v39
	v_mov_b32_e32 v39, v96
	v_fmac_f32_e32 v116, v45, v23
	v_fmac_f32_e32 v117, v49, v23
	v_fmac_f32_e32 v118, v53, v23
	ds_read_b128 v[16:19], v35
	ds_read_b128 v[4:7], v36
	v_fma_f32 v59, s4, v42, v114
	v_fma_f32 v94, v112, v42, v113
	ds_read_b128 v[44:47], v37
	ds_read_b128 v[48:51], v38
	ds_read_b128 v[52:55], v41
	v_fma_f32 v56, s4, v40, v114
	v_add_u32_e32 v120, 0xe0000, v96
	global_load_dword v120, v120, s[8:9] nt
	v_add_u32_e32 v121, 0xe4000, v96
	global_load_dword v121, v121, s[8:9] nt
	v_add_u32_e32 v126, 0xe8000, v96
	global_load_dword v126, v126, s[8:9] nt
	v_fma_f32 v40, v112, v40, v113
	v_fmamk_f32 v0, v8, 0x39800000, v0
	v_mul_f32_e32 v8, v56, v40
	v_mul_f32_e32 v8, 0xbfb8aa3b, v8
	v_exp_f32_e32 v8, v8
	v_fma_f32 v95, s4, v43, v114
	v_fma_f32 v43, v112, v43, v113
	v_fmac_f32_e32 v3, 0x39800000, v11
	v_add_f32_e32 v8, 1.0, v8
	v_rcp_f32_e32 v8, v8
	s_waitcnt vmcnt(3)
	v_add_f32_e32 v0, v0, v103
	v_add_u32_e32 v103, 0xec000, v96
	global_load_dword v103, v103, s[8:9] nt
	v_mul_f32_e32 v42, v0, v8
	v_fmamk_f32 v0, v9, 0x39800000, v1
	v_mul_f32_e32 v1, v57, v58
	v_mul_f32_e32 v1, 0xbfb8aa3b, v1
	v_exp_f32_e32 v1, v1
	v_add_f32_e32 v0, v0, v100
	s_waitcnt lgkmcnt(4)
	v_fmac_f32_e32 v115, v16, v42
	s_waitcnt lgkmcnt(2)
	v_fmac_f32_e32 v117, v44, v42
	v_add_f32_e32 v1, 1.0, v1
	v_rcp_f32_e32 v1, v1
	s_waitcnt lgkmcnt(1)
	v_fmac_f32_e32 v118, v48, v42
	v_or_b32_e32 v44, 56, v97
	v_fmac_f32_e32 v116, v4, v42
	v_mul_f32_e32 v40, v0, v1
	v_mul_f32_e32 v1, v59, v94
	v_mul_f32_e32 v1, 0xbfb8aa3b, v1
	v_exp_f32_e32 v1, v1
	v_fmamk_f32 v0, v10, 0x39800000, v2
	v_add_f32_e32 v0, v0, v101
	v_fmac_f32_e32 v115, v17, v40
	v_add_f32_e32 v1, 1.0, v1
	v_rcp_f32_e32 v1, v1
	v_fmac_f32_e32 v118, v49, v40
	v_lshlrev_b32_e32 v49, 2, v44
	v_or_b32_e32 v4, 0x10400, v49
	v_mul_f32_e32 v39, v0, v1
	v_mul_f32_e32 v0, v95, v43
	v_mul_f32_e32 v0, 0xbfb8aa3b, v0
	v_exp_f32_e32 v0, v0
	v_add_f32_e32 v1, v3, v102
	v_fmac_f32_e32 v115, v18, v39
	s_waitcnt lgkmcnt(0)
	v_fmac_f32_e32 v119, v52, v42
	v_add_f32_e32 v0, 1.0, v0
	v_rcp_f32_e32 v0, v0
	v_fmac_f32_e32 v117, v45, v40
	v_fmac_f32_e32 v116, v5, v40
	v_fmac_f32_e32 v119, v53, v40
	v_mul_f32_e32 v43, v1, v0
	v_or_b32_e32 v0, 0x10000, v49
	v_fmac_f32_e32 v115, v19, v43
	ds_read_b128 v[0:3], v0
	ds_read_b128 v[16:19], v4
	v_fmac_f32_e32 v117, v46, v39
	v_fmac_f32_e32 v116, v6, v39
	v_fmac_f32_e32 v118, v50, v39
	v_fmac_f32_e32 v119, v54, v39
	v_fmac_f32_e32 v117, v47, v43
	v_or_b32_e32 v45, 0x10800, v49
	v_or_b32_e32 v46, 0x10c00, v49
	v_or_b32_e32 v47, 0x11000, v49
	v_or_b32_e32 v48, 0x11400, v49
	v_or_b32_e32 v49, 0x11800, v49
	v_mov_b32_e32 v58, v96
	v_fmac_f32_e32 v116, v7, v43
	v_fmac_f32_e32 v118, v51, v43
	v_fmac_f32_e32 v119, v55, v43
	ds_read_b128 v[8:11], v45
	ds_read_b128 v[4:7], v46
	s_waitcnt lgkmcnt(3)
	v_fmamk_f32 v0, v12, 0x39800000, v0
	v_fmamk_f32 v1, v13, 0x39800000, v1
	v_fmamk_f32 v2, v14, 0x39800000, v2
	v_fmac_f32_e32 v3, 0x39800000, v15
	ds_read_b128 v[12:15], v47
	ds_read_b128 v[50:53], v48
	ds_read_b128 v[54:57], v49
	s_waitcnt lgkmcnt(5)
	v_fma_f32 v95, s4, v16, v114
	v_fma_f32 v16, v112, v16, v113
	v_mul_f32_e32 v16, v95, v16
	v_mul_f32_e32 v16, 0xbfb8aa3b, v16
	v_exp_f32_e32 v16, v16
	s_waitcnt vmcnt(3)
	v_add_f32_e32 v0, v0, v120
	v_add_f32_e32 v16, 1.0, v16
	v_rcp_f32_e32 v16, v16
	s_waitcnt vmcnt(2)
	v_add_f32_e32 v1, v1, v121
	v_mul_f32_e32 v16, v0, v16
	v_fma_f32 v0, s4, v17, v114
	v_fma_f32 v17, v112, v17, v113
	v_mul_f32_e32 v0, v0, v17
	v_mul_f32_e32 v0, 0xbfb8aa3b, v0
	v_exp_f32_e32 v0, v0
	s_waitcnt lgkmcnt(4)
	v_fmac_f32_e32 v115, v8, v16
	s_waitcnt lgkmcnt(3)
	v_fmac_f32_e32 v116, v4, v16
	s_waitcnt lgkmcnt(2)
	v_fmac_f32_e32 v117, v12, v16
	v_add_f32_e32 v0, 1.0, v0
	v_rcp_f32_e32 v0, v0
	s_waitcnt lgkmcnt(1)
	v_fmac_f32_e32 v118, v50, v16
	s_waitcnt lgkmcnt(0)
	v_fmac_f32_e32 v119, v54, v16
	v_mul_f32_e32 v17, v1, v0
	v_fma_f32 v0, s4, v18, v114
	v_fma_f32 v1, v112, v18, v113
	v_mul_f32_e32 v0, v0, v1
	v_mul_f32_e32 v0, 0xbfb8aa3b, v0
	v_exp_f32_e32 v0, v0
	s_waitcnt vmcnt(1)
	v_add_f32_e32 v1, v2, v126
	v_fmac_f32_e32 v114, s4, v19
	v_fmac_f32_e32 v113, v112, v19
	v_add_f32_e32 v0, 1.0, v0
	v_rcp_f32_e32 v0, v0
	v_fmac_f32_e32 v115, v9, v17
	v_fmac_f32_e32 v116, v5, v17
	v_fmac_f32_e32 v117, v13, v17
	v_mul_f32_e32 v18, v1, v0
	v_mul_f32_e32 v0, v114, v113
	v_mul_f32_e32 v0, 0xbfb8aa3b, v0
	v_exp_f32_e32 v0, v0
	s_waitcnt vmcnt(0)
	v_add_f32_e32 v1, v3, v103
	v_fmac_f32_e32 v118, v51, v17
	v_fmac_f32_e32 v119, v55, v17
	v_add_f32_e32 v0, 1.0, v0
	v_rcp_f32_e32 v0, v0
	v_fmac_f32_e32 v115, v10, v18
	v_fmac_f32_e32 v116, v6, v18
	v_fmac_f32_e32 v117, v14, v18
	v_mul_f32_e32 v19, v1, v0
	v_mbcnt_lo_u32_b32 v0, -1, 0
	v_mbcnt_hi_u32_b32 v0, -1, v0
	v_and_b32_e32 v2, 64, v0
	v_xor_b32_e32 v1, 32, v0
	v_add_u32_e32 v2, 64, v2
	v_cmp_lt_i32_e32 vcc, v1, v2
	v_fmac_f32_e32 v118, v52, v18
	v_fmac_f32_e32 v119, v56, v18
	v_cndmask_b32_e32 v0, v0, v1, vcc
	v_fmac_f32_e32 v115, v11, v19
	v_fmac_f32_e32 v116, v7, v19
	v_fmac_f32_e32 v117, v15, v19
	v_fmac_f32_e32 v118, v53, v19
	v_fmac_f32_e32 v119, v57, v19
	v_lshlrev_b32_e32 v50, 2, v0
	ds_bpermute_b32 v0, v50, v115
	ds_bpermute_b32 v1, v50, v116
	ds_bpermute_b32 v2, v50, v117
	ds_bpermute_b32 v3, v50, v118
	ds_bpermute_b32 v4, v50, v119
	v_cmp_gt_u32_e32 vcc, 32, v109
	s_and_saveexec_b64 s[4:5], vcc
	s_cbranch_execz .LBB13_8
	s_mul_i32 s7, s14, 0x280
	s_add_i32 s7, s6, s7
	s_waitcnt lgkmcnt(3)
	v_add_f32_e32 v1, v116, v1
	v_add_f32_e32 v0, v115, v0
	v_lshl_or_b32 v5, v98, 2, s7
	s_waitcnt lgkmcnt(0)
	v_add_f32_e32 v4, v119, v4
	v_add_f32_e32 v3, v118, v3
	v_add_f32_e32 v2, v117, v2
	ds_write2_b32 v5, v0, v1 offset1:32
	ds_write2_b32 v5, v2, v3 offset0:64 offset1:96
	ds_write_b32 v5, v4 offset:512
